# ret-scan: pipelined LDS fragment reads + 2-deep prefetch + LDS-staged wide O stores (fast path)
# speedup vs baseline: 1.0006x; 1.0006x over previous
; #define LAS __attribute__((address_space(3)))
; __device__ __forceinline__ void phase_ret_scan(const bf16* PROJ, bf16* O, LAS unsigned char* lds, int tid, int vcu, int G) {
;     ...
;         const int b = unit >> 6, h = (unit >> 3) & 7, vsl = unit & 7;
;         const float lg = __log2f(1.0f - exp2f(-5.0f - (float)h));
;         const float g64 = exp2f(64.0f * lg);
;         f32x16 S[2][2];
; #pragma unroll
;         for (int a = 0; a < 2; ++a)
; #pragma unroll
;             for (int c = 0; c < 2; ++c) S[a][c] = zero16();
;         for (int i = tid; i < 33792 / 16; i += 512) *(LAS v4u*)(lds + ST + i * 16) = (v4u){0u, 0u, 0u, 0u};
;         v4u pq[4], pk[4], pv;
;         const __amdgpu_buffer_rsrc_t rsP = __builtin_amdgcn_make_buffer_rsrc((void*)(PROJ + (size_t)b * SEQ * RT_IN), (short)0, SEQ * RT_IN * 2, 0x00020000);
;         const __amdgpu_buffer_rsrc_t rsO = __builtin_amdgcn_make_buffer_rsrc((void*)(O + (size_t)b * SEQ * RT_V), (short)0, SEQ * RT_V * 2, 0x00020000);
;         const int vrow = tid >> 3, vch = tid & 7;
;         const unsigned voq = (unsigned)((tid >> 5) * RT_IN + (tid & 31) * 8) * 2u, vov = (unsigned)(vrow * RT_IN + vch * 8) * 2u;
;         const unsigned soq = (unsigned)(h * 256) * 2u, sok = (unsigned)(2048 + h * 256) * 2u, sov = (unsigned)(4096 + h * 512 + vsl * 64) * 2u;
;     ...
;         RS_PREFETCH(0);
;         float dec[16];
;         { const int a31 = lane & 31, a5 = lane >> 5, w4 = wave & 3, t_i = w4 >> 1, x_i = w4 & 1;
; #pragma unroll
;           for (int r = 0; r < 16; ++r) {
;               if (wave < 4) { const int t = 32 * x_i + a31, s = 32 * t_i + 8 * (r >> 2) + 4 * a5 + (r & 3); dec[r] = (s <= t) ? __builtin_amdgcn_exp2f((float)(t - s) * lg) : 0.f; }
;               else { const int t = 32 * t_i + (r & 3) + 8 * (r >> 2) + 4 * a5; dec[r] = __builtin_amdgcn_exp2f((float)(t + 1) * lg); } } }
;         unsigned opk[8];
; #pragma unroll
;         for (int i = 0; i < 8; ++i) opk[i] = 0u;
.Lrf_636:
	s_ashr_i32 s27, s26, 31
	s_lshr_b32 s80, s79, 3
	s_lshl_b64 s[4:5], s[26:27], 25
	v_readlane_b32 s92, v250, 4
	s_add_u32 s92, s7, s4
	s_addc_u32 s81, s11, s5
	s_and_b32 s4, s80, 7
	s_lshl_b32 s5, s4, 10
	s_lshl_b32 s27, s4, 9
	v_mul_f32_e32 v2, 0x42800000, v0
	s_mov_b32 s4, 0xc2fc0000
	s_lshl_b32 s26, s78, 1
	v_cmp_gt_f32_e32 vcc, s4, v2
	s_and_b32 s26, s26, 0x380
	s_or_b32 s5, s5, s26
	v_cndmask_b32_e32 v2, 0, v197, vcc
	v_fmac_f32_e32 v2, 0x42800000, v0
	s_or_b32 s26, s5, 0x182000
	v_exp_f32_e32 v2, v2
	v_mul_f32_e32 v0, v0, v169
	v_readlane_b32 s93, v250, 5
	s_and_b64 s[4:5], vcc, exec
	v_exp_f32_e32 v150, v0
	v_readlane_b32 s94, v250, 6
	v_readlane_b32 s95, v250, 7
	s_cselect_b32 s4, 0xffffffc0, 0
	s_and_b32 s93, s81, 0xffff
	v_or_b32_e32 v0, s9, v170
	v_writelane_b32 v250, s92, 4
	v_or_b32_e32 v0, s8, v0
	v_mov_b32_e32 v14, v1
	v_mov_b32_e32 v15, v1
	v_ldexp_f32 v148, v2, s4
	v_writelane_b32 v250, s93, 5
	v_lshlrev_b32_e32 v224, 1, v0
	v_mov_b32_e32 v0, v1
	v_mov_b32_e32 v2, v1
	v_mov_b32_e32 v3, v1
	v_mov_b32_e32 v4, v1
	v_mov_b32_e32 v5, v1
	v_mov_b32_e32 v6, v1
	v_mov_b32_e32 v7, v1
	v_mov_b32_e32 v8, v1
	v_mov_b32_e32 v9, v1
	v_mov_b32_e32 v10, v1
	v_mov_b32_e32 v11, v1
	v_mov_b32_e32 v12, v1
	v_mov_b32_e32 v13, v1
	s_waitcnt vmcnt(13)
	v_mov_b64_e32 v[30:31], v[14:15]
	v_mov_b64_e32 v[46:47], v[14:15]
	v_mov_b64_e32 v[62:63], v[14:15]
	v_mov_b64_e32 v[78:79], v[14:15]
	s_mov_b32 s80, 0
	v_writelane_b32 v250, s94, 6
	v_mov_b32_e32 v151, v150
	v_mov_b32_e32 v152, v148
	v_mov_b32_e32 v153, v148
	v_mov_b32_e32 v225, 0
	v_mov_b32_e32 v226, 0
	v_mov_b32_e32 v227, 0
	v_mov_b32_e32 v228, 0
	v_mov_b32_e32 v229, 0
	v_mov_b32_e32 v230, 0
	v_mov_b32_e32 v231, 0
	v_mov_b32_e32 v232, 0
	s_mov_b32 s81, 0
	v_mov_b64_e32 v[28:29], v[12:13]
	v_mov_b64_e32 v[26:27], v[10:11]
	v_mov_b64_e32 v[24:25], v[8:9]
	v_mov_b64_e32 v[22:23], v[6:7]
	v_mov_b64_e32 v[20:21], v[4:5]
	v_mov_b64_e32 v[18:19], v[2:3]
	v_mov_b64_e32 v[16:17], v[0:1]
	v_mov_b64_e32 v[44:45], v[12:13]
	v_mov_b64_e32 v[42:43], v[10:11]
	v_mov_b64_e32 v[40:41], v[8:9]
	v_mov_b64_e32 v[38:39], v[6:7]
	v_mov_b64_e32 v[36:37], v[4:5]
	v_mov_b64_e32 v[34:35], v[2:3]
	v_mov_b64_e32 v[32:33], v[0:1]
	v_mov_b64_e32 v[60:61], v[12:13]
	v_mov_b64_e32 v[58:59], v[10:11]
	v_mov_b64_e32 v[56:57], v[8:9]
	v_mov_b64_e32 v[54:55], v[6:7]
	v_mov_b64_e32 v[52:53], v[4:5]
	v_mov_b64_e32 v[50:51], v[2:3]
	v_mov_b64_e32 v[48:49], v[0:1]
	v_mov_b64_e32 v[76:77], v[12:13]
	v_mov_b64_e32 v[74:75], v[10:11]
	v_mov_b64_e32 v[72:73], v[8:9]
	v_mov_b64_e32 v[70:71], v[6:7]
	v_mov_b64_e32 v[68:69], v[4:5]
	v_mov_b64_e32 v[66:67], v[2:3]
	v_mov_b64_e32 v[64:65], v[0:1]
	v_writelane_b32 v250, s95, 7
	s_nop 1
	v_readlane_b32 s92, v250, 0
	v_readlane_b32 s93, v250, 1
	v_readlane_b32 s94, v250, 2
	v_readlane_b32 s95, v250, 3
	s_add_i32 s4, s27, 0x180000
	s_add_i32 s5, s27, 0x181000
	s_nop 4
	buffer_load_dwordx4 v[170:173], v167, s[92:95], s4 offen
	buffer_load_dwordx4 v[174:177], v167, s[92:95], s5 offen
	s_add_i32 s4, s27, 0x1e0000
	s_add_i32 s5, s27, 0x1e1000
	buffer_load_dwordx4 v[178:181], v167, s[92:95], s4 offen
	buffer_load_dwordx4 v[182:185], v167, s[92:95], s5 offen
	s_add_i32 s4, s27, 0x240000
	s_add_i32 s5, s27, 0x241000
	buffer_load_dwordx4 v[186:189], v167, s[92:95], s4 offen
	buffer_load_dwordx4 v[202:205], v167, s[92:95], s5 offen
	s_add_i32 s4, s27, 0x2a0000
	s_add_i32 s5, s27, 0x2a1000
	buffer_load_dwordx4 v[206:209], v167, s[92:95], s4 offen
	buffer_load_dwordx4 v[238:241], v167, s[92:95], s5 offen
	buffer_load_dwordx4 v[244:247], v168, s[92:95], s26 offen
	v_lshrrev_b32_e32 v191, 3, v165
	v_and_b32_e32 v190, 7, v165
	v_lshlrev_b32_e32 v201, 13, v191
	v_lshl_add_u32 v201, v190, 4, v201
	s_add_i32 s4, s8, s9
	s_lshl_b32 s4, s4, 1
	v_add_u32_e32 v201, s4, v201
	v_mul_u32_u24_e32 v191, 0x90, v191
	v_lshl_add_u32 v191, v190, 4, v191
	v_add_u32_e32 v191, 0x21000, v191
	v_bfe_u32 v190, v165, 5, 1
	v_lshl_add_u32 v190, v190, 2, s12
	v_mul_u32_u24_e32 v190, 0x90, v190
	v_and_b32_e32 v169, 31, v165
	v_add_u32_e32 v169, s13, v169
	v_lshl_add_u32 v190, v169, 1, v190
	v_add_u32_e32 v190, 0x21000, v190
	s_branch .Lrf_639

; #define LAS __attribute__((address_space(3)))
; __device__ __forceinline__ v4u scale_bf8(v4u q, float f) { v4u o; o.x = pk2(bflo(q.x) * f, bfhi(q.x) * f); o.y = pk2(bflo(q.y) * f, bfhi(q.y) * f); o.z = pk2(bflo(q.z) * f, bfhi(q.z) * f); o.w = pk2(bflo(q.w) * f, bfhi(q.w) * f); return o; }
; __device__ __forceinline__ void phase_ret_scan(const bf16* PROJ, bf16* O, LAS unsigned char* lds, int tid, int vcu, int G) {
;     ...
;         for (int ch = 0; ch < SEQ / 64; ++ch) {
; #pragma unroll
;             for (int i = 0; i < 4; ++i) { const int cid = tid + 512 * i, row = cid >> 5, chq = cid & 31;
;                 *(LAS v4u*)(lds + QN + row * QRS + chq * 16) = pq[i];
;                 *(LAS v4u*)(lds + KN + (chq >> 4) * 16384 + off_b(row, chq & 15)) = pk[i]; }
;             *(LAS v4u*)(lds + VV + off_b(vrow, vch)) = pv;
;             *(LAS v4u*)(lds + VV + off_b(vrow, 8 + vch)) = scale_bf8(pv, __builtin_amdgcn_exp2f((float)(63 - vrow) * lg));
;             __syncthreads();
;     ...
;             if (ch > 0) RS_STORE_O(ch - 1);
.Lrf_639:
	s_bitcmp1_b32 s81, 19
	s_cbranch_scc1 .Lrf_topB
	s_waitcnt vmcnt(9)
	s_cmp_eq_u32 s81, 0
	s_cbranch_scc1 .Lrf_noOrdA
	ds_read_b128 v[8:11], v191
.Lrf_noOrdA:
	v_lshlrev_b32_e32 v2, 16, v128
	v_and_b32_e32 v3, 0xffff0000, v128
	v_lshlrev_b32_e32 v4, 16, v129
	v_and_b32_e32 v5, 0xffff0000, v129
	v_pk_mul_f32 v[2:3], v[150:151], v[2:3]
	v_pk_mul_f32 v[4:5], v[150:151], v[4:5]
	s_cmp_lg_u32 s81, 0
	v_cvt_pk_bf16_f32 v2, v2, v3
	v_cvt_pk_bf16_f32 v3, v4, v5
	v_lshlrev_b32_e32 v4, 16, v130
	v_and_b32_e32 v5, 0xffff0000, v130
	v_lshlrev_b32_e32 v6, 16, v131
	v_and_b32_e32 v7, 0xffff0000, v131
	s_cselect_b64 s[4:5], -1, 0
	v_pk_mul_f32 v[4:5], v[150:151], v[4:5]
	v_pk_mul_f32 v[6:7], v[150:151], v[6:7]
	v_cvt_pk_bf16_f32 v4, v4, v5
	v_cvt_pk_bf16_f32 v5, v6, v7
	s_and_b64 vcc, exec, s[4:5]
	ds_write_b128 v214, v[96:99]
	ds_write_b128 v215, v[100:103] offset:33792
	ds_write_b128 v216, v[104:107]
	ds_write_b128 v217, v[108:111] offset:33792
	ds_write_b128 v218, v[112:115]
	ds_write_b128 v219, v[116:119] offset:33792
	ds_write_b128 v220, v[120:123]
	ds_write_b128 v221, v[124:127] offset:33792
	ds_write_b128 v222, v[128:131]
	ds_write_b128 v223, v[2:5]
	s_waitcnt lgkmcnt(0)
	s_barrier
	s_cbranch_vccz .Lrf_641A
	s_add_i32 s5, s81, 0xfff80000
	v_readlane_b32 s92, v250, 4
	v_readlane_b32 s93, v250, 5
	v_readlane_b32 s94, v250, 6
	v_readlane_b32 s95, v250, 7
	s_nop 4
	buffer_store_dwordx4 v[8:11], v201, s[92:95], s5 offen

; #define LAS __attribute__((address_space(3)))
; __device__ __forceinline__ v4u scale_bf8(v4u q, float f) { v4u o; o.x = pk2(bflo(q.x) * f, bfhi(q.x) * f); o.y = pk2(bflo(q.y) * f, bfhi(q.y) * f); o.z = pk2(bflo(q.z) * f, bfhi(q.z) * f); o.w = pk2(bflo(q.w) * f, bfhi(q.w) * f); return o; }
; __device__ __forceinline__ void phase_ret_scan(const bf16* PROJ, bf16* O, LAS unsigned char* lds, int tid, int vcu, int G) {
;     ...
;         for (int ch = 0; ch < SEQ / 64; ++ch) {
; #pragma unroll
;             for (int i = 0; i < 4; ++i) { const int cid = tid + 512 * i, row = cid >> 5, chq = cid & 31;
;                 *(LAS v4u*)(lds + QN + row * QRS + chq * 16) = pq[i];
;                 *(LAS v4u*)(lds + KN + (chq >> 4) * 16384 + off_b(row, chq & 15)) = pk[i]; }
;             *(LAS v4u*)(lds + VV + off_b(vrow, vch)) = pv;
;             *(LAS v4u*)(lds + VV + off_b(vrow, 8 + vch)) = scale_bf8(pv, __builtin_amdgcn_exp2f((float)(63 - vrow) * lg));
;             __syncthreads();
;     ...
;             if (ch > 0) RS_STORE_O(ch - 1);
.Lrf_topB_go:
	ds_read_b128 v[8:11], v191
	v_lshlrev_b32_e32 v2, 16, v244
	v_and_b32_e32 v3, 0xffff0000, v244
	v_lshlrev_b32_e32 v4, 16, v245
	v_and_b32_e32 v5, 0xffff0000, v245
	v_pk_mul_f32 v[2:3], v[150:151], v[2:3]
	v_pk_mul_f32 v[4:5], v[150:151], v[4:5]
	s_cmp_lg_u32 s81, 0
	v_cvt_pk_bf16_f32 v2, v2, v3
	v_cvt_pk_bf16_f32 v3, v4, v5
	v_lshlrev_b32_e32 v4, 16, v246
	v_and_b32_e32 v5, 0xffff0000, v246
	v_lshlrev_b32_e32 v6, 16, v247
	v_and_b32_e32 v7, 0xffff0000, v247
	s_cselect_b64 s[4:5], -1, 0
	v_pk_mul_f32 v[4:5], v[150:151], v[4:5]
	v_pk_mul_f32 v[6:7], v[150:151], v[6:7]
	v_cvt_pk_bf16_f32 v4, v4, v5
	v_cvt_pk_bf16_f32 v5, v6, v7
	s_and_b64 vcc, exec, s[4:5]
	ds_write_b128 v214, v[170:173]
	ds_write_b128 v215, v[174:177] offset:33792
	ds_write_b128 v216, v[178:181]
	ds_write_b128 v217, v[182:185] offset:33792
	ds_write_b128 v218, v[186:189]
	ds_write_b128 v219, v[202:205] offset:33792
	ds_write_b128 v220, v[206:209]
	ds_write_b128 v221, v[238:241] offset:33792
	ds_write_b128 v222, v[244:247]
	ds_write_b128 v223, v[2:5]
	s_waitcnt lgkmcnt(0)
	s_barrier
	s_cbranch_vccz .Lrf_641B
	s_add_i32 s5, s81, 0xfff80000
	v_readlane_b32 s92, v250, 4
	v_readlane_b32 s93, v250, 5
	v_readlane_b32 s94, v250, 6
	v_readlane_b32 s95, v250, 7
	s_nop 4
	buffer_store_dwordx4 v[8:11], v201, s[92:95], s5 offen

; __device__ __forceinline__ unsigned pk2(float lo, float hi) { const pk_f2 v = {lo, hi}; return __builtin_bit_cast(unsigned, __builtin_convertvector(v, pk_b2)); }
; #define RS_MMA4(fa, fb) do { _Pragma("unroll") for (int j = 0; j < 4; ++j) acc = mfma32(fa[j], fb[j], acc); } while (0)
; __device__ __forceinline__ void phase_ret_scan(const bf16* PROJ, bf16* O, LAS unsigned char* lds, int tid, int vcu, int G) {
;     ...
;                 RS_MMA4(fa0, fb0);
; #pragma unroll
;                 for (int i = 0; i < 8; ++i) { const float o0_ = acc[2 * i], o1_ = acc[2 * i + 1]; opk[i] = pk2(o0_, o1_); }
;             }
;     ...
;             __syncthreads();
;         }
;         RS_STORE_O(SEQ / 64 - 1);
.Lrf_649:
	s_andn2_b64 vcc, exec, s[8:9]
	s_cbranch_vccz .Lrf_637
	ds_write_b16 v190, v4
	ds_write_b16_d16_hi v190, v4 offset:144
	ds_write_b16 v190, v5 offset:288
	ds_write_b16_d16_hi v190, v5 offset:432
	ds_write_b16 v190, v6 offset:1152
	ds_write_b16_d16_hi v190, v6 offset:1296
	ds_write_b16 v190, v7 offset:1440
	ds_write_b16_d16_hi v190, v7 offset:1584
	ds_write_b16 v190, v8 offset:2304
	ds_write_b16_d16_hi v190, v8 offset:2448
	ds_write_b16 v190, v9 offset:2592
	ds_write_b16_d16_hi v190, v9 offset:2736
	ds_write_b16 v190, v10 offset:3456
	ds_write_b16_d16_hi v190, v10 offset:3600
	ds_write_b16 v190, v11 offset:3744
	ds_write_b16_d16_hi v190, v11 offset:3888
	s_branch .Lrf_638
.Lrf_651:
	ds_read_b128 v[8:11], v191
	v_readlane_b32 s80, v250, 4
	v_readlane_b32 s81, v250, 5
	v_readlane_b32 s82, v250, 6
	v_readlane_b32 s83, v250, 7
	s_mov_b32 s5, 0x1f80000
	s_waitcnt lgkmcnt(0)
	s_nop 4
	buffer_store_dwordx4 v[8:11], v201, s[80:83], s5 offen
	s_branch .LBB0_568
